# converter walk: one counted wait per transpose (vmcnt 24 while loads keep coming) instead of hipcc's draining ladders
# baseline (speedup 1.0000x reference)
; #define GAS __attribute__((address_space(1)))
; #define P0_GET() do { if (DYN) { int v_ = 0x7fffffff; if (lane == 0) { if (!check_stop || __hip_atomic_load(stopw, RLX_AGENT) == 0u) v_ = (int)atomicAdd(qword, 1u); } \
;         idx = __builtin_amdgcn_readfirstlane(v_); ok = idx < P0_NHALF; } else { idx = cur_static; cur_static += nw; ok = idx < s1; } } while (0)
; #define P0_MAKE() (DYN ? p0_strip_half(args, ws, idx) : p0_strip(args, ws, idx))
; __device__ __forceinline__ void p0_load(f32x4 (&v)[8], const Strip& st, int j, int lane) {
;     const float* p = st.src + (size_t)(j * 64 + (lane >> 3)) * st.ldw + (lane & 7) * 4;
; #pragma unroll
;     for (int i = 0; i < 8; ++i) v[i] = __builtin_nontemporal_load((const GAS f32x4*)(p + (size_t)(i * 8) * st.ldw));
; }
; template <bool DYN>
; __device__ __forceinline__ void p0_walk(const Args& args, unsigned char* ws, LAS float* scr, int lane, int w, int nw, int s0, int s1, unsigned* qword, unsigned* stopw, bool check_stop) {
;     ...
;     P0_GET();
;     if (!ok) return;
;     Strip lst = P0_MAKE(), sst = lst, nst = lst; bool has_n = false, lv = true, sv = true; int lj = 0, sj = 0;
;     f32x4 b0[8], b1[8], b2[8], b3[8]; u32x2 hold[4];
.LBB0_35:
	s_andn2_b64 vcc, exec, s[48:49]
	s_cbranch_vccnz .LBB0_53
	v_lshl_or_b32 v130, s3, 6, v133
	v_lshlrev_b64 v[74:75], 13, v[130:131]
	v_lshl_add_u64 v[74:75], s[44:45], 0, v[74:75]
	v_lshlrev_b32_e32 v130, 2, v132
	v_lshl_add_u64 v[118:119], v[74:75], 0, v[130:131]
	v_add_co_u32_e32 v78, vcc, 0x10000, v118
	s_add_i32 s3, s3, 1
	s_nop 0
	v_addc_co_u32_e32 v79, vcc, 0, v119, vcc
	v_add_co_u32_e32 v90, vcc, 0x20000, v118
	global_load_dwordx4 v[74:77], v[118:119], off nt
	s_nop 0
	global_load_dwordx4 v[78:81], v[78:79], off nt
	v_addc_co_u32_e32 v91, vcc, 0, v119, vcc
	v_add_co_u32_e32 v94, vcc, 0x30000, v118
	s_cmp_lg_u32 s3, 8
	s_nop 0
	v_addc_co_u32_e32 v95, vcc, 0, v119, vcc
	v_add_co_u32_e32 v106, vcc, 0x40000, v118
	global_load_dwordx4 v[90:93], v[90:91], off nt
	s_nop 0
	global_load_dwordx4 v[94:97], v[94:95], off nt
	v_addc_co_u32_e32 v107, vcc, 0, v119, vcc
	v_add_co_u32_e32 v110, vcc, 0x50000, v118
	s_mov_b64 s[48:49], -1
	s_nop 0
	v_addc_co_u32_e32 v111, vcc, 0, v119, vcc
	v_add_co_u32_e32 v120, vcc, 0x60000, v118
	global_load_dwordx4 v[106:109], v[106:107], off nt
	s_nop 0
	global_load_dwordx4 v[110:113], v[110:111], off nt
	v_addc_co_u32_e32 v121, vcc, 0, v119, vcc
	v_add_co_u32_e32 v126, vcc, 0x70000, v118
	s_nop 1
	v_addc_co_u32_e32 v127, vcc, 0, v119, vcc
	global_load_dwordx4 v[118:121], v[120:121], off nt
	s_nop 0
	global_load_dwordx4 v[126:129], v[126:127], off nt
	s_cbranch_scc1 .LBB0_54
	v_bfrev_b32_e32 v130, -2
	s_and_saveexec_b64 s[48:49], s[4:5]
	s_cbranch_execz .LBB0_42
	global_load_dword v130, v131, s[6:7] sc1
	s_waitcnt vmcnt(0)
	v_cmp_ne_u32_e32 vcc, 0, v130
	v_bfrev_b32_e32 v130, -2
	s_cbranch_vccnz .LBB0_42
	s_mov_b64 s[54:55], exec
	v_mbcnt_lo_u32_b32 v130, s54, 0
	v_mbcnt_hi_u32_b32 v130, s55, v130
	v_cmp_eq_u32_e32 vcc, 0, v130
	s_and_saveexec_b64 s[50:51], vcc
	s_cbranch_execz .LBB0_41
	s_bcnt1_i32_b64 s3, s[54:55]
	s_waitcnt lgkmcnt(0)
	v_mov_b32_e32 v136, s3
	global_atomic_add v136, v131, v136, s[8:9] sc0

; #define P0_LD(B_) do { if (lv) { p0_load(B_, lst, lj, lane); if (++lj == lst.nk) { lj = 0; P0_GET(); if (ok) { lst = P0_MAKE(); nst = lst; has_n = true; } else lv = false; } } } while (0)
; #define P0_ST(B_, ODD_) do { p0_store<ODD_>(B_, sst, sj, scr, lane, hold); if (++sj == sst.nk) { sj = 0; if (has_n) { sst = nst; has_n = false; } else sv = false; } } while (0)
; template <bool DYN>
; __device__ __forceinline__ void p0_walk(const Args& args, unsigned char* ws, LAS float* scr, int lane, int w, int nw, int s0, int s1, unsigned* qword, unsigned* stopw, bool check_stop) {
;     ...
;     P0_LD(b0); P0_LD(b1); P0_LD(b2);
;     while (sv) {
;         P0_LD(b3); P0_ST(b0, false); if (!sv) break;
;         P0_LD(b0); P0_ST(b1, true); if (!sv) break;
;         P0_LD(b1); P0_ST(b2, false); if (!sv) break;
;         P0_LD(b2); P0_ST(b3, true);
.LBB0_54:
	s_and_b64 vcc, exec, s[48:49]
	s_cbranch_vccz .Lcvw0_drain
	s_waitcnt vmcnt(24)
	s_branch .Lcvw0_go

; #define GAS __attribute__((address_space(1)))
; #define LAS __attribute__((address_space(3)))
; #define LDS_WAIT() asm volatile("s_waitcnt lgkmcnt(0)" ::: "memory")
; __device__ __forceinline__ unsigned cvtpk(float lo, float hi) { unsigned r; asm volatile("v_cvt_pk_bf16_f32 %0, %1, %2" : "=v"(r) : "v"(lo), "v"(hi)); return r; }
; __device__ __forceinline__ unsigned cvt4_fp8(float a, float b, float c, float d) { int w = 0; w = __builtin_amdgcn_cvt_pk_fp8_f32(a, b, w, false); w = __builtin_amdgcn_cvt_pk_fp8_f32(c, d, w, true); return (unsigned)w; }
; template <bool ODD> __device__ __forceinline__ void p0_store(const f32x4 (&v)[8], const Strip& st, int j, LAS float* scr, int lane, u32x2 (&hold)[4]) {
; #pragma unroll
;     for (int i = 0; i < 8; ++i) { LAS float* sp = scr + (i * 8 + (lane >> 3)) * 33 + (lane & 7) * 4; sp[0] = v[i][0]; sp[1] = v[i][1]; sp[2] = v[i][2]; sp[3] = v[i][3]; }
;     LDS_WAIT(); asm volatile("" ::: "memory");
;     const int c = lane & 7;
; #pragma unroll
;     for (int jj = 0; jj < 4; ++jj) { const int n = (lane >> 3) + 8 * jj; const LAS float* sp = scr + (8 * c) * 33 + n;
;         const float a0 = sp[0 * 33], a1 = sp[1 * 33], a2 = sp[2 * 33], a3 = sp[3 * 33], a4 = sp[4 * 33], a5 = sp[5 * 33], a6 = sp[6 * 33], a7 = sp[7 * 33];
;         unsigned char* rowp = st.dst + (size_t)map_row_rt(st.mode, st.n0 + n) * st.Kb;
;         if (st.out8) { u32x2 o; o.x = cvt4_fp8(a0 * 64.f, a1 * 64.f, a2 * 64.f, a3 * 64.f); o.y = cvt4_fp8(a4 * 64.f, a5 * 64.f, a6 * 64.f, a7 * 64.f);
;             if constexpr (!ODD) hold[jj] = o; else { __builtin_nontemporal_store(hold[jj], (GAS u32x2*)(rowp + (j - 1) * 64 + 8 * c)); __builtin_nontemporal_store(o, (GAS u32x2*)(rowp + j * 64 + 8 * c)); } }
;         else { f32x4 g0 = {1.f, 1.f, 1.f, 1.f}, g1 = g0; if (st.gain) { g0 = *(const f32x4*)(st.gain + j * 64 + 8 * c); g1 = *(const f32x4*)(st.gain + j * 64 + 8 * c + 4); }
;             u32x4 o; o.x = cvtpk(a0 * g0[0], a1 * g0[1]); o.y = cvtpk(a2 * g0[2], a3 * g0[3]); o.z = cvtpk(a4 * g1[0], a5 * g1[1]); o.w = cvtpk(a6 * g1[2], a7 * g1[3]); *(GAS u32x4*)(rowp + j * 128 + 16 * c) = o; } }
;     LDS_WAIT(); asm volatile("" ::: "memory");
.Lcvw0_go:
	v_add_u32_e32 v185, 0x420, v184
	v_add_u32_e32 v186, 0x428, v184
	v_add_u32_e32 v187, 0x840, v184
	v_add_u32_e32 v188, 0x848, v184
	v_add_u32_e32 v189, 0xc60, v184
	v_add_u32_e32 v190, 0xc68, v184
	v_add_u32_e32 v191, 0x1080, v184
	v_add_u32_e32 v192, 0x1088, v184
	v_add_u32_e32 v193, 0x14a0, v184
	v_add_u32_e32 v194, 0x14a8, v184
	v_add_u32_e32 v195, 0x18c0, v184
	v_add_u32_e32 v196, 0x18c8, v184
	v_add_u32_e32 v197, 0x1ce0, v184
	v_add_u32_e32 v198, 0x1ce8, v184
	ds_write2_b32 v184, v2, v3 offset1:1
	ds_write2_b32 v184, v4, v5 offset0:2 offset1:3
	ds_write2_b32 v185, v6, v7 offset1:1
	ds_write2_b32 v186, v8, v9 offset1:1
	ds_write2_b32 v187, v10, v11 offset1:1
	ds_write2_b32 v188, v12, v13 offset1:1
	ds_write2_b32 v189, v14, v15 offset1:1
	ds_write2_b32 v190, v16, v17 offset1:1
	ds_write2_b32 v191, v18, v19 offset1:1
	ds_write2_b32 v192, v20, v21 offset1:1
	ds_write2_b32 v193, v22, v23 offset1:1
	ds_write2_b32 v194, v24, v25 offset1:1
	ds_write2_b32 v195, v26, v27 offset1:1
	ds_write2_b32 v196, v28, v29 offset1:1
	ds_write2_b32 v197, v30, v31 offset1:1
	ds_write2_b32 v198, v32, v33 offset1:1
	s_waitcnt lgkmcnt(0)
	s_waitcnt lgkmcnt(0)
	ds_read2_b32 v[160:161], v183 offset1:8
	ds_read2_b32 v[162:163], v183 offset0:33 offset1:41
	ds_read2_b32 v[168:169], v183 offset0:66 offset1:74
	ds_read2_b32 v[170:171], v183 offset0:99 offset1:107
	ds_read2_b32 v[156:157], v183 offset0:132 offset1:140
	ds_read2_b32 v[158:159], v183 offset0:165 offset1:173
	ds_read2_b32 v[152:153], v183 offset0:198 offset1:206
	ds_read2_b32 v[154:155], v183 offset0:231 offset1:239
	ds_read2_b32 v[144:145], v183 offset0:16 offset1:24
	ds_read2_b32 v[146:147], v183 offset0:49 offset1:57
	ds_read2_b32 v[148:149], v183 offset0:82 offset1:90
	ds_read2_b32 v[150:151], v183 offset0:115 offset1:123
	ds_read2_b32 v[140:141], v183 offset0:148 offset1:156
	ds_read2_b32 v[142:143], v183 offset0:181 offset1:189
	ds_read2_b32 v[136:137], v183 offset0:214 offset1:222
	ds_read2_b32 v[138:139], v183 offset0:247 offset1:255
	s_waitcnt lgkmcnt(0)
	s_add_i32 s26, s26, 1
	s_cmp_lg_u32 s26, 8
	s_cselect_b64 s[54:55], -1, 0
	s_and_b64 vcc, exec, s[54:55]
	s_cbranch_vccnz .LBB0_56
	s_mov_b32 s26, 0
	s_mov_b64 s[50:51], 0
	s_mov_b64 s[42:43], s[46:47]
	s_mov_b32 s16, s68
	s_mov_b32 s17, s69
	s_andn2_b64 vcc, exec, s[52:53]
	s_mov_b64 s[54:55], -1
	s_cbranch_vccnz .LBB0_34
	s_branch .LBB0_57

; #define GAS __attribute__((address_space(1)))
; #define LAS __attribute__((address_space(3)))
; #define LDS_WAIT() asm volatile("s_waitcnt lgkmcnt(0)" ::: "memory")
; __device__ __forceinline__ unsigned cvtpk(float lo, float hi) { unsigned r; asm volatile("v_cvt_pk_bf16_f32 %0, %1, %2" : "=v"(r) : "v"(lo), "v"(hi)); return r; }
; __device__ __forceinline__ unsigned cvt4_fp8(float a, float b, float c, float d) { int w = 0; w = __builtin_amdgcn_cvt_pk_fp8_f32(a, b, w, false); w = __builtin_amdgcn_cvt_pk_fp8_f32(c, d, w, true); return (unsigned)w; }
; template <bool ODD> __device__ __forceinline__ void p0_store(const f32x4 (&v)[8], const Strip& st, int j, LAS float* scr, int lane, u32x2 (&hold)[4]) {
; #pragma unroll
;     for (int i = 0; i < 8; ++i) { LAS float* sp = scr + (i * 8 + (lane >> 3)) * 33 + (lane & 7) * 4; sp[0] = v[i][0]; sp[1] = v[i][1]; sp[2] = v[i][2]; sp[3] = v[i][3]; }
;     LDS_WAIT(); asm volatile("" ::: "memory");
;     const int c = lane & 7;
; #pragma unroll
;     for (int jj = 0; jj < 4; ++jj) { const int n = (lane >> 3) + 8 * jj; const LAS float* sp = scr + (8 * c) * 33 + n;
;         const float a0 = sp[0 * 33], a1 = sp[1 * 33], a2 = sp[2 * 33], a3 = sp[3 * 33], a4 = sp[4 * 33], a5 = sp[5 * 33], a6 = sp[6 * 33], a7 = sp[7 * 33];
;         unsigned char* rowp = st.dst + (size_t)map_row_rt(st.mode, st.n0 + n) * st.Kb;
;         if (st.out8) { u32x2 o; o.x = cvt4_fp8(a0 * 64.f, a1 * 64.f, a2 * 64.f, a3 * 64.f); o.y = cvt4_fp8(a4 * 64.f, a5 * 64.f, a6 * 64.f, a7 * 64.f);
;             if constexpr (!ODD) hold[jj] = o; else { __builtin_nontemporal_store(hold[jj], (GAS u32x2*)(rowp + (j - 1) * 64 + 8 * c)); __builtin_nontemporal_store(o, (GAS u32x2*)(rowp + j * 64 + 8 * c)); } }
;         else { f32x4 g0 = {1.f, 1.f, 1.f, 1.f}, g1 = g0; if (st.gain) { g0 = *(const f32x4*)(st.gain + j * 64 + 8 * c); g1 = *(const f32x4*)(st.gain + j * 64 + 8 * c + 4); }
;             u32x4 o; o.x = cvtpk(a0 * g0[0], a1 * g0[1]); o.y = cvtpk(a2 * g0[2], a3 * g0[3]); o.z = cvtpk(a4 * g1[0], a5 * g1[1]); o.w = cvtpk(a6 * g1[2], a7 * g1[3]); *(GAS u32x4*)(rowp + j * 128 + 16 * c) = o; } }
;     LDS_WAIT(); asm volatile("" ::: "memory");
.Lcvw1_go:
	ds_write2_b32 v184, v34, v35 offset1:1
	ds_write2_b32 v184, v36, v37 offset0:2 offset1:3
	ds_write2_b32 v185, v38, v39 offset1:1
	ds_write2_b32 v186, v40, v41 offset1:1
	ds_write2_b32 v187, v42, v43 offset1:1
	ds_write2_b32 v188, v44, v45 offset1:1
	ds_write2_b32 v189, v46, v47 offset1:1
	ds_write2_b32 v190, v48, v49 offset1:1
	ds_write2_b32 v191, v50, v51 offset1:1
	ds_write2_b32 v192, v52, v53 offset1:1
	ds_write2_b32 v193, v54, v55 offset1:1
	ds_write2_b32 v194, v56, v57 offset1:1
	ds_write2_b32 v195, v58, v59 offset1:1
	ds_write2_b32 v196, v60, v61 offset1:1
	ds_write2_b32 v197, v62, v63 offset1:1
	ds_write2_b32 v198, v64, v65 offset1:1
	s_waitcnt lgkmcnt(0)
	ds_read2_b32 v[178:179], v183 offset1:33
	ds_read2_b32 v[176:177], v183 offset0:66 offset1:99
	ds_read2_b32 v[174:175], v183 offset0:132 offset1:165
	ds_read2_b32 v[172:173], v183 offset0:198 offset1:231
	v_add_u32_e32 v130, s17, v133
	s_cmp_lt_i32 s16, 3
	s_mov_b64 s[52:53], -1
	s_cbranch_scc1 .LBB0_83
	s_cmp_lt_i32 s16, 4
	s_cbranch_scc1 .LBB0_80
	s_cmp_eq_u32 s16, 4
	v_mov_b32_e32 v180, v130
	s_cbranch_scc0 .LBB0_79
	v_lshlrev_b32_e32 v180, 1, v130
	v_and_b32_e32 v180, 0x7fffff00, v180
	v_and_b32_e32 v181, 0x7f, v130
	v_or3_b32 v180, v181, v180, s63

; #define GAS __attribute__((address_space(1)))
; #define LAS __attribute__((address_space(3)))
; #define LDS_WAIT() asm volatile("s_waitcnt lgkmcnt(0)" ::: "memory")
; __device__ __forceinline__ unsigned cvtpk(float lo, float hi) { unsigned r; asm volatile("v_cvt_pk_bf16_f32 %0, %1, %2" : "=v"(r) : "v"(lo), "v"(hi)); return r; }
; __device__ __forceinline__ unsigned cvt4_fp8(float a, float b, float c, float d) { int w = 0; w = __builtin_amdgcn_cvt_pk_fp8_f32(a, b, w, false); w = __builtin_amdgcn_cvt_pk_fp8_f32(c, d, w, true); return (unsigned)w; }
; template <bool ODD> __device__ __forceinline__ void p0_store(const f32x4 (&v)[8], const Strip& st, int j, LAS float* scr, int lane, u32x2 (&hold)[4]) {
; #pragma unroll
;     for (int i = 0; i < 8; ++i) { LAS float* sp = scr + (i * 8 + (lane >> 3)) * 33 + (lane & 7) * 4; sp[0] = v[i][0]; sp[1] = v[i][1]; sp[2] = v[i][2]; sp[3] = v[i][3]; }
;     LDS_WAIT(); asm volatile("" ::: "memory");
;     const int c = lane & 7;
; #pragma unroll
;     for (int jj = 0; jj < 4; ++jj) { const int n = (lane >> 3) + 8 * jj; const LAS float* sp = scr + (8 * c) * 33 + n;
;         const float a0 = sp[0 * 33], a1 = sp[1 * 33], a2 = sp[2 * 33], a3 = sp[3 * 33], a4 = sp[4 * 33], a5 = sp[5 * 33], a6 = sp[6 * 33], a7 = sp[7 * 33];
;         unsigned char* rowp = st.dst + (size_t)map_row_rt(st.mode, st.n0 + n) * st.Kb;
;         if (st.out8) { u32x2 o; o.x = cvt4_fp8(a0 * 64.f, a1 * 64.f, a2 * 64.f, a3 * 64.f); o.y = cvt4_fp8(a4 * 64.f, a5 * 64.f, a6 * 64.f, a7 * 64.f);
;             if constexpr (!ODD) hold[jj] = o; else { __builtin_nontemporal_store(hold[jj], (GAS u32x2*)(rowp + (j - 1) * 64 + 8 * c)); __builtin_nontemporal_store(o, (GAS u32x2*)(rowp + j * 64 + 8 * c)); } }
;         else { f32x4 g0 = {1.f, 1.f, 1.f, 1.f}, g1 = g0; if (st.gain) { g0 = *(const f32x4*)(st.gain + j * 64 + 8 * c); g1 = *(const f32x4*)(st.gain + j * 64 + 8 * c + 4); }
;             u32x4 o; o.x = cvtpk(a0 * g0[0], a1 * g0[1]); o.y = cvtpk(a2 * g0[2], a3 * g0[3]); o.z = cvtpk(a4 * g1[0], a5 * g1[1]); o.w = cvtpk(a6 * g1[2], a7 * g1[3]); *(GAS u32x4*)(rowp + j * 128 + 16 * c) = o; } }
;     LDS_WAIT(); asm volatile("" ::: "memory");
.Lcvw2_go:
	ds_write2_b32 v184, v66, v67 offset1:1
	ds_write2_b32 v184, v68, v69 offset0:2 offset1:3
	ds_write2_b32 v185, v70, v71 offset1:1
	ds_write2_b32 v186, v72, v73 offset1:1
	ds_write2_b32 v187, v82, v83 offset1:1
	ds_write2_b32 v188, v84, v85 offset1:1
	ds_write2_b32 v189, v86, v87 offset1:1
	ds_write2_b32 v190, v88, v89 offset1:1
	ds_write2_b32 v191, v98, v99 offset1:1
	ds_write2_b32 v192, v100, v101 offset1:1
	ds_write2_b32 v193, v102, v103 offset1:1
	ds_write2_b32 v194, v104, v105 offset1:1
	ds_write2_b32 v195, v114, v115 offset1:1
	ds_write2_b32 v196, v116, v117 offset1:1
	ds_write2_b32 v197, v122, v123 offset1:1
	ds_write2_b32 v198, v124, v125 offset1:1
	s_waitcnt lgkmcnt(0)
	ds_read2_b32 v[160:161], v183 offset1:8
	ds_read2_b32 v[162:163], v183 offset0:33 offset1:41
	ds_read2_b32 v[168:169], v183 offset0:66 offset1:74
	ds_read2_b32 v[170:171], v183 offset0:99 offset1:107
	ds_read2_b32 v[156:157], v183 offset0:132 offset1:140
	ds_read2_b32 v[158:159], v183 offset0:165 offset1:173
	ds_read2_b32 v[152:153], v183 offset0:198 offset1:206
	ds_read2_b32 v[154:155], v183 offset0:231 offset1:239
	ds_read2_b32 v[144:145], v183 offset0:16 offset1:24
	ds_read2_b32 v[146:147], v183 offset0:49 offset1:57
	ds_read2_b32 v[148:149], v183 offset0:82 offset1:90
	ds_read2_b32 v[150:151], v183 offset0:115 offset1:123
	ds_read2_b32 v[140:141], v183 offset0:148 offset1:156
	ds_read2_b32 v[142:143], v183 offset0:181 offset1:189
	ds_read2_b32 v[136:137], v183 offset0:214 offset1:222
	ds_read2_b32 v[138:139], v183 offset0:247 offset1:255
	s_waitcnt lgkmcnt(0)
	s_add_i32 s26, s26, 1
	s_cmp_lg_u32 s26, 8
	s_cselect_b64 s[54:55], -1, 0
	s_and_b64 vcc, exec, s[54:55]
	s_cbranch_vccnz .LBB0_192
	s_mov_b32 s26, 0
	s_mov_b64 s[50:51], 0
	s_mov_b64 s[42:43], s[46:47]
	s_mov_b32 s16, s68
	s_mov_b32 s17, s69
	s_andn2_b64 vcc, exec, s[52:53]
	s_mov_b64 s[54:55], -1
	s_cbranch_vccz .LBB0_193

; #define GAS __attribute__((address_space(1)))
; #define LAS __attribute__((address_space(3)))
; #define LDS_WAIT() asm volatile("s_waitcnt lgkmcnt(0)" ::: "memory")
; __device__ __forceinline__ unsigned cvtpk(float lo, float hi) { unsigned r; asm volatile("v_cvt_pk_bf16_f32 %0, %1, %2" : "=v"(r) : "v"(lo), "v"(hi)); return r; }
; __device__ __forceinline__ unsigned cvt4_fp8(float a, float b, float c, float d) { int w = 0; w = __builtin_amdgcn_cvt_pk_fp8_f32(a, b, w, false); w = __builtin_amdgcn_cvt_pk_fp8_f32(c, d, w, true); return (unsigned)w; }
; template <bool ODD> __device__ __forceinline__ void p0_store(const f32x4 (&v)[8], const Strip& st, int j, LAS float* scr, int lane, u32x2 (&hold)[4]) {
; #pragma unroll
;     for (int i = 0; i < 8; ++i) { LAS float* sp = scr + (i * 8 + (lane >> 3)) * 33 + (lane & 7) * 4; sp[0] = v[i][0]; sp[1] = v[i][1]; sp[2] = v[i][2]; sp[3] = v[i][3]; }
;     LDS_WAIT(); asm volatile("" ::: "memory");
;     const int c = lane & 7;
; #pragma unroll
;     for (int jj = 0; jj < 4; ++jj) { const int n = (lane >> 3) + 8 * jj; const LAS float* sp = scr + (8 * c) * 33 + n;
;         const float a0 = sp[0 * 33], a1 = sp[1 * 33], a2 = sp[2 * 33], a3 = sp[3 * 33], a4 = sp[4 * 33], a5 = sp[5 * 33], a6 = sp[6 * 33], a7 = sp[7 * 33];
;         unsigned char* rowp = st.dst + (size_t)map_row_rt(st.mode, st.n0 + n) * st.Kb;
;         if (st.out8) { u32x2 o; o.x = cvt4_fp8(a0 * 64.f, a1 * 64.f, a2 * 64.f, a3 * 64.f); o.y = cvt4_fp8(a4 * 64.f, a5 * 64.f, a6 * 64.f, a7 * 64.f);
;             if constexpr (!ODD) hold[jj] = o; else { __builtin_nontemporal_store(hold[jj], (GAS u32x2*)(rowp + (j - 1) * 64 + 8 * c)); __builtin_nontemporal_store(o, (GAS u32x2*)(rowp + j * 64 + 8 * c)); } }
;         else { f32x4 g0 = {1.f, 1.f, 1.f, 1.f}, g1 = g0; if (st.gain) { g0 = *(const f32x4*)(st.gain + j * 64 + 8 * c); g1 = *(const f32x4*)(st.gain + j * 64 + 8 * c + 4); }
;             u32x4 o; o.x = cvtpk(a0 * g0[0], a1 * g0[1]); o.y = cvtpk(a2 * g0[2], a3 * g0[3]); o.z = cvtpk(a4 * g1[0], a5 * g1[1]); o.w = cvtpk(a6 * g1[2], a7 * g1[3]); *(GAS u32x4*)(rowp + j * 128 + 16 * c) = o; } }
;     LDS_WAIT(); asm volatile("" ::: "memory");
.Lcvw3_drain:
	s_waitcnt vmcnt(0)
.Lcvw3_go:
	ds_write2_b32 v184, v74, v75 offset1:1
	ds_write2_b32 v184, v76, v77 offset0:2 offset1:3
	ds_write2_b32 v185, v78, v79 offset1:1
	ds_write2_b32 v186, v80, v81 offset1:1
	ds_write2_b32 v187, v90, v91 offset1:1
	ds_write2_b32 v188, v92, v93 offset1:1
	ds_write2_b32 v189, v94, v95 offset1:1
	ds_write2_b32 v190, v96, v97 offset1:1
	ds_write2_b32 v191, v106, v107 offset1:1
	ds_write2_b32 v192, v108, v109 offset1:1
	ds_write2_b32 v193, v110, v111 offset1:1
	ds_write2_b32 v194, v112, v113 offset1:1
	ds_write2_b32 v195, v118, v119 offset1:1
	ds_write2_b32 v196, v120, v121 offset1:1
	ds_write2_b32 v197, v126, v127 offset1:1
	ds_write2_b32 v198, v128, v129 offset1:1
	s_waitcnt lgkmcnt(0)
	ds_read2_b32 v[178:179], v183 offset1:33
	ds_read2_b32 v[176:177], v183 offset0:66 offset1:99
	ds_read2_b32 v[174:175], v183 offset0:132 offset1:165
	ds_read2_b32 v[172:173], v183 offset0:198 offset1:231
	v_add_u32_e32 v130, s17, v133
	s_cmp_lt_i32 s16, 3
	s_mov_b64 s[52:53], -1
	s_cbranch_scc1 .LBB0_219
	s_cmp_lt_i32 s16, 4
	s_cbranch_scc1 .LBB0_216
	s_cmp_eq_u32 s16, 4
	v_mov_b32_e32 v180, v130
	s_cbranch_scc0 .LBB0_215
	v_lshlrev_b32_e32 v180, 1, v130
	v_and_b32_e32 v180, 0x7fffff00, v180
	v_and_b32_e32 v181, 0x7f, v130
	v_or3_b32 v180, v181, v180, s63
